# v79 + accumulator clearing between GEMM tiles with 64-bit moves (945 fewer instructions)
# speedup vs baseline: 1.0122x; 1.0006x over previous
.LBB0_104:
	v_mov_b32_e32 v2, 0
	s_mov_b32 s38, s93
	s_mov_b32 s91, s92
	v_mov_b32_e32 v3, v2
	v_mov_b64_e32 v[4:5], v[2:3]
	v_mov_b64_e32 v[6:7], v[2:3]
	v_mov_b64_e32 v[8:9], v[2:3]
	v_mov_b64_e32 v[10:11], v[2:3]
	v_mov_b64_e32 v[12:13], v[2:3]
	v_mov_b64_e32 v[14:15], v[2:3]
	v_mov_b64_e32 v[16:17], v[2:3]
	v_mov_b64_e32 v[18:19], v[2:3]
	v_mov_b64_e32 v[20:21], v[2:3]
	v_mov_b64_e32 v[22:23], v[2:3]
	v_mov_b64_e32 v[24:25], v[2:3]
	v_mov_b64_e32 v[26:27], v[2:3]
	v_mov_b64_e32 v[28:29], v[2:3]
	v_mov_b64_e32 v[30:31], v[2:3]
	v_mov_b64_e32 v[32:33], v[2:3]
	v_mov_b64_e32 v[34:35], v[2:3]
	v_mov_b64_e32 v[36:37], v[2:3]
	v_mov_b64_e32 v[38:39], v[2:3]
	v_mov_b64_e32 v[40:41], v[2:3]
	v_mov_b64_e32 v[42:43], v[2:3]
	v_mov_b64_e32 v[44:45], v[2:3]
	v_mov_b64_e32 v[46:47], v[2:3]
	v_mov_b64_e32 v[48:49], v[2:3]
	v_mov_b64_e32 v[50:51], v[2:3]
	v_mov_b64_e32 v[52:53], v[2:3]
	v_mov_b64_e32 v[54:55], v[2:3]
	v_mov_b64_e32 v[56:57], v[2:3]
	v_mov_b64_e32 v[58:59], v[2:3]
	v_mov_b64_e32 v[60:61], v[2:3]
	v_mov_b64_e32 v[62:63], v[2:3]
	v_mov_b64_e32 v[64:65], v[2:3]
	v_mov_b64_e32 v[66:67], v[2:3]
	v_mov_b64_e32 v[68:69], v[2:3]
	v_mov_b64_e32 v[70:71], v[2:3]
	v_mov_b64_e32 v[72:73], v[2:3]
	v_mov_b64_e32 v[74:75], v[2:3]
	v_mov_b64_e32 v[76:77], v[2:3]
	v_mov_b64_e32 v[78:79], v[2:3]
	v_mov_b64_e32 v[80:81], v[2:3]
	v_mov_b64_e32 v[82:83], v[2:3]
	v_mov_b64_e32 v[84:85], v[2:3]
	v_mov_b64_e32 v[86:87], v[2:3]
	v_mov_b64_e32 v[88:89], v[2:3]
	v_mov_b64_e32 v[90:91], v[2:3]
	v_mov_b64_e32 v[92:93], v[2:3]
	v_mov_b64_e32 v[94:95], v[2:3]
	v_mov_b64_e32 v[96:97], v[2:3]
	v_mov_b64_e32 v[98:99], v[2:3]
	v_mov_b64_e32 v[100:101], v[2:3]
	v_mov_b64_e32 v[102:103], v[2:3]
	v_mov_b64_e32 v[104:105], v[2:3]
	v_mov_b64_e32 v[106:107], v[2:3]
	v_mov_b64_e32 v[108:109], v[2:3]
	v_mov_b64_e32 v[110:111], v[2:3]
	v_mov_b64_e32 v[112:113], v[2:3]
	v_mov_b64_e32 v[114:115], v[2:3]
	v_mov_b64_e32 v[116:117], v[2:3]
	v_mov_b64_e32 v[118:119], v[2:3]
	v_mov_b64_e32 v[120:121], v[2:3]
	v_mov_b64_e32 v[122:123], v[2:3]
	v_mov_b64_e32 v[124:125], v[2:3]
	v_mov_b64_e32 v[126:127], v[2:3]
	v_mov_b64_e32 v[128:129], v[2:3]
	s_andn2_b64 vcc, exec, s[40:41]
	s_cbranch_vccnz .LBB0_86

.LBB0_356:
	s_ashr_i32 s57, s56, 31
	s_lshl_b64 s[60:61], s[56:57], 19
	v_readlane_b32 s29, v253, 49
	s_add_u32 s60, s29, s60
	v_readlane_b32 s29, v253, 50
	s_addc_u32 s61, s29, s61
	s_and_b64 s[64:65], s[62:63], exec
	s_cselect_b32 s29, s61, s41
	s_cselect_b32 s37, s60, s40
	s_ashr_i32 s59, s58, 31
	s_lshl_b64 s[64:65], s[58:59], 19
	v_readlane_b32 s39, v253, 52
	s_add_u32 s64, s39, s64
	v_readlane_b32 s39, v253, 53
	s_addc_u32 s65, s39, s65
	s_and_b64 s[82:83], s[62:63], exec
	s_cselect_b32 s39, s65, s67
	s_cselect_b32 s57, s64, s66
	s_add_u32 s40, s40, 0x40080
	s_addc_u32 s41, s41, 0
	s_add_u32 s59, s66, 0x100
	v_mov_b32_e32 v2, 0
	s_addc_u32 vcc_lo, s67, 0
	s_mov_b32 vcc_hi, -2
	v_mov_b32_e32 v3, v2
	v_mov_b64_e32 v[4:5], v[2:3]
	v_mov_b64_e32 v[6:7], v[2:3]
	v_mov_b64_e32 v[8:9], v[2:3]
	v_mov_b64_e32 v[10:11], v[2:3]
	v_mov_b64_e32 v[12:13], v[2:3]
	v_mov_b64_e32 v[14:15], v[2:3]
	v_mov_b64_e32 v[16:17], v[2:3]
	v_mov_b64_e32 v[18:19], v[2:3]
	v_mov_b64_e32 v[20:21], v[2:3]
	v_mov_b64_e32 v[22:23], v[2:3]
	v_mov_b64_e32 v[24:25], v[2:3]
	v_mov_b64_e32 v[26:27], v[2:3]
	v_mov_b64_e32 v[28:29], v[2:3]
	v_mov_b64_e32 v[30:31], v[2:3]
	v_mov_b64_e32 v[32:33], v[2:3]
	v_mov_b64_e32 v[34:35], v[2:3]
	v_mov_b64_e32 v[36:37], v[2:3]
	v_mov_b64_e32 v[38:39], v[2:3]
	v_mov_b64_e32 v[40:41], v[2:3]
	v_mov_b64_e32 v[42:43], v[2:3]
	v_mov_b64_e32 v[44:45], v[2:3]
	v_mov_b64_e32 v[54:55], v[2:3]
	v_mov_b64_e32 v[56:57], v[2:3]
	v_mov_b64_e32 v[66:67], v[2:3]
	v_mov_b64_e32 v[68:69], v[2:3]
	v_mov_b64_e32 v[70:71], v[2:3]
	v_mov_b64_e32 v[72:73], v[2:3]
	v_mov_b64_e32 v[90:91], v[2:3]
	v_mov_b64_e32 v[92:93], v[2:3]
	v_mov_b64_e32 v[94:95], v[2:3]
	v_mov_b64_e32 v[96:97], v[2:3]
	v_mov_b64_e32 v[98:99], v[2:3]
	v_mov_b64_e32 v[100:101], v[2:3]
	v_mov_b64_e32 v[102:103], v[2:3]
	v_mov_b64_e32 v[104:105], v[2:3]
	v_mov_b64_e32 v[106:107], v[2:3]
	v_mov_b64_e32 v[108:109], v[2:3]
	v_mov_b64_e32 v[110:111], v[2:3]
	v_mov_b64_e32 v[112:113], v[2:3]
	v_mov_b64_e32 v[114:115], v[2:3]
	v_mov_b64_e32 v[116:117], v[2:3]
	v_mov_b64_e32 v[118:119], v[2:3]
	v_mov_b64_e32 v[120:121], v[2:3]
	v_mov_b64_e32 v[122:123], v[2:3]
	v_mov_b64_e32 v[124:125], v[2:3]
	v_mov_b64_e32 v[126:127], v[2:3]
	v_mov_b64_e32 v[128:129], v[2:3]
	v_mov_b64_e32 v[130:131], v[2:3]
	v_mov_b64_e32 v[132:133], v[2:3]
	v_mov_b64_e32 v[134:135], v[2:3]
	v_mov_b64_e32 v[136:137], v[2:3]
	v_mov_b64_e32 v[138:139], v[2:3]
	v_mov_b64_e32 v[140:141], v[2:3]
	v_mov_b64_e32 v[142:143], v[2:3]
	v_mov_b64_e32 v[144:145], v[2:3]
	v_mov_b64_e32 v[146:147], v[2:3]
	v_mov_b64_e32 v[148:149], v[2:3]
	v_mov_b64_e32 v[150:151], v[2:3]
	v_mov_b64_e32 v[152:153], v[2:3]
	v_mov_b64_e32 v[154:155], v[2:3]
	v_mov_b64_e32 v[156:157], v[2:3]
	v_mov_b64_e32 v[158:159], v[2:3]
	v_mov_b64_e32 v[160:161], v[2:3]

.LBB0_403:
	v_mov_b32_e32 v2, 0
	s_mov_b32 s16, s40
	s_mov_b32 s88, s38
	v_mov_b32_e32 v3, v2
	v_mov_b64_e32 v[4:5], v[2:3]
	v_mov_b64_e32 v[6:7], v[2:3]
	v_mov_b64_e32 v[8:9], v[2:3]
	v_mov_b64_e32 v[10:11], v[2:3]
	v_mov_b64_e32 v[12:13], v[2:3]
	v_mov_b64_e32 v[14:15], v[2:3]
	v_mov_b64_e32 v[16:17], v[2:3]
	v_mov_b64_e32 v[18:19], v[2:3]
	v_mov_b64_e32 v[20:21], v[2:3]
	v_mov_b64_e32 v[22:23], v[2:3]
	v_mov_b64_e32 v[24:25], v[2:3]
	v_mov_b64_e32 v[26:27], v[2:3]
	v_mov_b64_e32 v[28:29], v[2:3]
	v_mov_b64_e32 v[30:31], v[2:3]
	v_mov_b64_e32 v[32:33], v[2:3]
	v_mov_b64_e32 v[34:35], v[2:3]
	v_mov_b64_e32 v[36:37], v[2:3]
	v_mov_b64_e32 v[38:39], v[2:3]
	v_mov_b64_e32 v[40:41], v[2:3]
	v_mov_b64_e32 v[42:43], v[2:3]
	v_mov_b64_e32 v[44:45], v[2:3]
	v_mov_b64_e32 v[46:47], v[2:3]
	v_mov_b64_e32 v[48:49], v[2:3]
	v_mov_b64_e32 v[50:51], v[2:3]
	v_mov_b64_e32 v[52:53], v[2:3]
	v_mov_b64_e32 v[54:55], v[2:3]
	v_mov_b64_e32 v[56:57], v[2:3]
	v_mov_b64_e32 v[58:59], v[2:3]
	v_mov_b64_e32 v[60:61], v[2:3]
	v_mov_b64_e32 v[62:63], v[2:3]
	v_mov_b64_e32 v[64:65], v[2:3]
	v_mov_b64_e32 v[66:67], v[2:3]
	v_mov_b64_e32 v[68:69], v[2:3]
	v_mov_b64_e32 v[70:71], v[2:3]
	v_mov_b64_e32 v[72:73], v[2:3]
	v_mov_b64_e32 v[74:75], v[2:3]
	v_mov_b64_e32 v[76:77], v[2:3]
	v_mov_b64_e32 v[78:79], v[2:3]
	v_mov_b64_e32 v[80:81], v[2:3]
	v_mov_b64_e32 v[82:83], v[2:3]
	v_mov_b64_e32 v[84:85], v[2:3]
	v_mov_b64_e32 v[86:87], v[2:3]
	v_mov_b64_e32 v[88:89], v[2:3]
	v_mov_b64_e32 v[90:91], v[2:3]
	v_mov_b64_e32 v[92:93], v[2:3]
	v_mov_b64_e32 v[94:95], v[2:3]
	v_mov_b64_e32 v[96:97], v[2:3]
	v_mov_b64_e32 v[98:99], v[2:3]
	v_mov_b64_e32 v[100:101], v[2:3]
	v_mov_b64_e32 v[102:103], v[2:3]
	v_mov_b64_e32 v[104:105], v[2:3]
	v_mov_b64_e32 v[106:107], v[2:3]
	v_mov_b64_e32 v[108:109], v[2:3]
	v_mov_b64_e32 v[110:111], v[2:3]
	v_mov_b64_e32 v[112:113], v[2:3]
	v_mov_b64_e32 v[114:115], v[2:3]
	v_mov_b64_e32 v[116:117], v[2:3]
	v_mov_b64_e32 v[118:119], v[2:3]
	v_mov_b64_e32 v[120:121], v[2:3]
	v_mov_b64_e32 v[122:123], v[2:3]
	v_mov_b64_e32 v[124:125], v[2:3]
	v_mov_b64_e32 v[126:127], v[2:3]
	v_mov_b64_e32 v[128:129], v[2:3]
	s_andn2_b64 vcc, exec, s[42:43]
	s_cbranch_vccnz .LBB0_387

.LBB0_428:
	v_or_b32_e32 v160, s1, v6
	v_lshl_add_u64 v[10:11], s[48:49], 0, v[0:1]
	v_mov_b32_e32 v143, v1
	s_and_b32 s31, s29, 3
	v_and_b32_e32 v4, 48, v4
	v_lshlrev_b32_e32 v18, 6, v160
	s_movk_i32 s29, 0x3c0
	v_lshlrev_b32_e32 v19, 2, v160
	s_add_i32 s66, s58, 0x18000
	v_lshl_add_u64 v[12:13], s[48:49], 0, v[142:143]
	v_mov_b32_e32 v149, v1
	v_and_or_b32 v18, v18, s29, v4
	s_lshl_b32 s0, s0, 13
	v_and_b32_e32 v19, 32, v19
	v_lshl_add_u64 v[10:11], v[10:11], 0, s[18:19]
	s_mov_b32 m0, s66
	s_add_i32 s67, s58, 0x1a000
	v_lshl_add_u64 v[14:15], s[16:17], 0, v[148:149]
	v_mov_b32_e32 v145, v1
	v_bitop3_b32 v161, v18, s0, v19 bitop3:0xde
	s_lshl_b32 s0, s31, 12
	s_waitcnt vmcnt(2)
	s_barrier
	global_load_lds_dwordx4 v[10:11], off
	v_lshl_add_u64 v[10:11], v[12:13], 0, s[18:19]
	s_mov_b32 m0, s67
	s_add_i32 s80, s58, 0x8000
	s_add_i32 s82, s58, 0xa000
	v_lshl_add_u64 v[16:17], s[16:17], 0, v[144:145]
	global_load_lds_dwordx4 v[10:11], off
	v_lshl_add_u64 v[10:11], v[14:15], 0, s[18:19]
	s_mov_b32 m0, s80
	s_add_u32 s36, s48, 0x40080
	global_load_lds_dwordx4 v[10:11], off
	v_lshl_add_u64 v[10:11], v[16:17], 0, s[18:19]
	s_mov_b32 m0, s82
	s_addc_u32 s37, s49, 0
	s_add_i32 s83, s58, 0x1c000
	global_load_lds_dwordx4 v[10:11], off
	v_lshl_add_u64 v[10:11], s[36:37], 0, v[0:1]
	s_mov_b32 m0, s83
	s_add_i32 s84, s58, 0x1e000
	global_load_lds_dwordx4 v[10:11], off
	v_lshl_add_u64 v[10:11], s[36:37], 0, v[142:143]
	s_mov_b32 m0, s84
	v_lshl_or_b32 v4, v6, 6, v4
	global_load_lds_dwordx4 v[10:11], off
	v_lshlrev_b32_e32 v6, 2, v6
	v_and_b32_e32 v6, 32, v6
	v_bitop3_b32 v162, v4, s0, v6 bitop3:0xde
	v_lshlrev_b32_e32 v4, 14, v8
	v_and_b32_e32 v4, 0xffff8000, v4
	v_lshl_add_u32 v4, v7, 11, v4
	v_and_b32_e32 v6, 1, v8
	v_lshl_or_b32 v4, v6, 6, v4
	v_lshl_add_u32 v152, v9, 1, v4
	v_lshlrev_b32_e32 v4, 14, v2
	v_and_b32_e32 v4, 0xffff8000, v4
	v_lshl_add_u32 v3, v3, 11, v4
	v_and_b32_e32 v2, 1, v2
	v_readlane_b32 s36, v252, 7
	s_waitcnt vmcnt(6)
	v_lshl_or_b32 v2, v2, 6, v3
	v_readlane_b32 s37, v252, 8
	v_lshl_add_u32 v154, v5, 1, v2
	v_mov_b32_e32 v2, 0
	s_mov_b32 s0, s36
	v_readlane_b32 s36, v252, 3
	v_mov_b32_e32 v153, v1
	v_mov_b32_e32 v155, v1
	s_mov_b32 s85, 0
	s_mov_b32 s34, s36
	v_mov_b32_e32 v3, v2
	v_mov_b64_e32 v[4:5], v[2:3]
	v_mov_b64_e32 v[6:7], v[2:3]
	v_mov_b64_e32 v[8:9], v[2:3]
	v_mov_b64_e32 v[10:11], v[2:3]
	v_mov_b64_e32 v[12:13], v[2:3]
	v_mov_b64_e32 v[14:15], v[2:3]
	v_mov_b64_e32 v[16:17], v[2:3]
	v_mov_b64_e32 v[18:19], v[2:3]
	v_mov_b64_e32 v[20:21], v[2:3]
	v_mov_b64_e32 v[22:23], v[2:3]
	v_mov_b64_e32 v[24:25], v[2:3]
	v_mov_b64_e32 v[26:27], v[2:3]
	v_mov_b64_e32 v[28:29], v[2:3]
	v_mov_b64_e32 v[30:31], v[2:3]
	v_mov_b64_e32 v[32:33], v[2:3]
	v_mov_b64_e32 v[34:35], v[2:3]
	v_mov_b64_e32 v[36:37], v[2:3]
	v_mov_b64_e32 v[38:39], v[2:3]
	v_mov_b64_e32 v[40:41], v[2:3]
	v_mov_b64_e32 v[42:43], v[2:3]
	v_mov_b64_e32 v[44:45], v[2:3]
	v_mov_b64_e32 v[46:47], v[2:3]
	v_mov_b64_e32 v[48:49], v[2:3]
	v_mov_b64_e32 v[50:51], v[2:3]
	v_mov_b64_e32 v[52:53], v[2:3]
	v_mov_b64_e32 v[54:55], v[2:3]
	v_mov_b64_e32 v[56:57], v[2:3]
	v_mov_b64_e32 v[58:59], v[2:3]
	v_mov_b64_e32 v[60:61], v[2:3]
	v_mov_b64_e32 v[62:63], v[2:3]
	v_mov_b64_e32 v[64:65], v[2:3]
	v_mov_b64_e32 v[66:67], v[2:3]
	v_mov_b64_e32 v[68:69], v[2:3]
	v_mov_b64_e32 v[70:71], v[2:3]
	v_mov_b64_e32 v[72:73], v[2:3]
	v_mov_b64_e32 v[74:75], v[2:3]
	v_mov_b64_e32 v[76:77], v[2:3]
	v_mov_b64_e32 v[78:79], v[2:3]
	v_mov_b64_e32 v[80:81], v[2:3]
	v_mov_b64_e32 v[82:83], v[2:3]
	v_mov_b64_e32 v[84:85], v[2:3]
	v_mov_b64_e32 v[86:87], v[2:3]
	v_mov_b64_e32 v[88:89], v[2:3]
	v_mov_b64_e32 v[90:91], v[2:3]
	v_mov_b64_e32 v[92:93], v[2:3]
	v_mov_b64_e32 v[94:95], v[2:3]
	v_mov_b64_e32 v[96:97], v[2:3]
	v_mov_b64_e32 v[98:99], v[2:3]
	v_mov_b64_e32 v[100:101], v[2:3]
	v_mov_b64_e32 v[102:103], v[2:3]
	v_mov_b64_e32 v[104:105], v[2:3]
	v_mov_b64_e32 v[106:107], v[2:3]
	v_mov_b64_e32 v[108:109], v[2:3]
	v_mov_b64_e32 v[110:111], v[2:3]
	v_mov_b64_e32 v[112:113], v[2:3]
	v_mov_b64_e32 v[114:115], v[2:3]
	v_mov_b64_e32 v[116:117], v[2:3]
	v_mov_b64_e32 v[118:119], v[2:3]
	v_mov_b64_e32 v[120:121], v[2:3]
	v_mov_b64_e32 v[122:123], v[2:3]
	v_mov_b64_e32 v[124:125], v[2:3]
	v_mov_b64_e32 v[126:127], v[2:3]
	v_mov_b64_e32 v[128:129], v[2:3]
	s_barrier
	v_readlane_b32 s37, v252, 4

.LBB0_438:
	v_or_b32_e32 v163, 0x10000, v162
	v_add_u32_e32 v168, 0x10400, v162
	ds_read_b128 v[164:167], v163
	ds_read_b128 v[168:171], v168
	v_add_u32_e32 v163, 0x10800, v162
	v_add_u32_e32 v176, 0x10c00, v162
	s_add_u32 s50, s16, s48
	ds_read_b128 v[172:175], v163
	ds_read_b128 v[176:179], v176
	v_or_b32_e32 v163, 0x14000, v162
	v_add_u32_e32 v184, 0x14400, v162
	s_addc_u32 s51, s17, s49
	ds_read_b128 v[180:183], v163
	ds_read_b128 v[184:187], v184
	v_add_u32_e32 v163, 0x14800, v162
	v_add_u32_e32 v192, 0x14c00, v162
	s_add_u32 s50, s50, 0x100
	ds_read_b128 v[188:191], v163
	ds_read_b128 v[192:195], v192
	s_addc_u32 s51, s51, 0
	s_add_u32 s91, s41, s48
	s_addc_u32 s92, s89, s49
	s_cmpk_eq_i32 s48, 0x700
	s_cselect_b32 s53, s29, s51
	s_cselect_b32 s52, s39, s50
	s_cselect_b32 s51, s45, s92
	s_cselect_b32 s50, s44, s91
	v_lshl_add_u64 v[226:227], v[156:157], 0, s[48:49]
	s_add_i32 m0, s58, 0xc000
	ds_read_b128 v[200:203], v161
	ds_read_b128 v[204:207], v161 offset:1024
	ds_read_b128 v[208:211], v161 offset:2048
	ds_read_b128 v[212:215], v161 offset:3072
	ds_read_b128 v[216:219], v161 offset:4096
	ds_read_b128 v[220:223], v161 offset:5120
	ds_read_b128 v[236:239], v161 offset:6144
	ds_read_b128 v[240:243], v161 offset:7168
	global_load_lds_dwordx4 v[226:227], off
	v_lshl_add_u64 v[226:227], v[158:159], 0, s[48:49]
	s_add_i32 m0, s58, 0xe000
	s_nop 0
	global_load_lds_dwordx4 v[226:227], off
	s_waitcnt vmcnt(8)
	s_waitcnt lgkmcnt(0)
	s_barrier
	s_setprio 1
	s_waitcnt lgkmcnt(0)
	v_mfma_f32_16x16x32_bf16 v[126:129], v[164:167], v[200:203], v[126:129]
	v_mfma_f32_16x16x32_bf16 v[122:125], v[172:175], v[200:203], v[122:125]
	v_mfma_f32_16x16x32_bf16 v[110:113], v[164:167], v[208:211], v[110:113]
	v_mfma_f32_16x16x32_bf16 v[106:109], v[172:175], v[208:211], v[106:109]
	v_mfma_f32_16x16x32_bf16 v[94:97], v[164:167], v[216:219], v[94:97]
	v_mfma_f32_16x16x32_bf16 v[90:93], v[172:175], v[216:219], v[90:93]
	v_mfma_f32_16x16x32_bf16 v[86:89], v[164:167], v[236:239], v[86:89]
	v_mfma_f32_16x16x32_bf16 v[78:81], v[172:175], v[236:239], v[78:81]
	v_mfma_f32_16x16x32_bf16 v[126:129], v[168:171], v[204:207], v[126:129]
	v_mfma_f32_16x16x32_bf16 v[122:125], v[176:179], v[204:207], v[122:125]
	v_mfma_f32_16x16x32_bf16 v[110:113], v[168:171], v[212:215], v[110:113]
	v_mfma_f32_16x16x32_bf16 v[106:109], v[176:179], v[212:215], v[106:109]
	v_mfma_f32_16x16x32_bf16 v[94:97], v[168:171], v[220:223], v[94:97]
	v_mfma_f32_16x16x32_bf16 v[90:93], v[176:179], v[220:223], v[90:93]
	v_mfma_f32_16x16x32_bf16 v[86:89], v[168:171], v[240:243], v[86:89]
	v_mfma_f32_16x16x32_bf16 v[78:81], v[176:179], v[240:243], v[78:81]
	s_setprio 0
	s_setprio 1
	v_mfma_f32_16x16x32_bf16 v[118:121], v[180:183], v[200:203], v[118:121]
	v_mfma_f32_16x16x32_bf16 v[114:117], v[188:191], v[200:203], v[114:117]
	v_mfma_f32_16x16x32_bf16 v[102:105], v[180:183], v[208:211], v[102:105]
	v_mfma_f32_16x16x32_bf16 v[98:101], v[188:191], v[208:211], v[98:101]
	v_mfma_f32_16x16x32_bf16 v[82:85], v[180:183], v[216:219], v[82:85]
	v_mfma_f32_16x16x32_bf16 v[74:77], v[188:191], v[216:219], v[74:77]
	v_mfma_f32_16x16x32_bf16 v[70:73], v[180:183], v[236:239], v[70:73]
	v_mfma_f32_16x16x32_bf16 v[66:69], v[188:191], v[236:239], v[66:69]
	v_mfma_f32_16x16x32_bf16 v[118:121], v[184:187], v[204:207], v[118:121]
	v_mfma_f32_16x16x32_bf16 v[114:117], v[192:195], v[204:207], v[114:117]
	v_mfma_f32_16x16x32_bf16 v[102:105], v[184:187], v[212:215], v[102:105]
	v_mfma_f32_16x16x32_bf16 v[98:101], v[192:195], v[212:215], v[98:101]
	v_mfma_f32_16x16x32_bf16 v[82:85], v[184:187], v[220:223], v[82:85]
	v_mfma_f32_16x16x32_bf16 v[74:77], v[192:195], v[220:223], v[74:77]
	v_mfma_f32_16x16x32_bf16 v[70:73], v[184:187], v[240:243], v[70:73]
	v_mfma_f32_16x16x32_bf16 v[66:69], v[192:195], v[240:243], v[66:69]
	s_setprio 0
	s_barrier
	s_mov_b32 m0, s59
	v_lshl_add_u64 v[226:227], s[50:51], 0, v[0:1]
	s_add_u32 s92, s50, 0x40000
	ds_read_b128 v[200:203], v161 offset:16384
	ds_read_b128 v[204:207], v161 offset:17408
	ds_read_b128 v[208:211], v161 offset:18432
	ds_read_b128 v[212:215], v161 offset:19456
	ds_read_b128 v[216:219], v161 offset:20480
	ds_read_b128 v[220:223], v161 offset:21504
	ds_read_b128 v[236:239], v161 offset:22528
	ds_read_b128 v[240:243], v161 offset:23552
	global_load_lds_dwordx4 v[226:227], off
	v_lshl_add_u64 v[244:245], s[50:51], 0, v[142:143]
	s_mov_b32 m0, s60
	s_addc_u32 s93, s51, 0
	global_load_lds_dwordx4 v[244:245], off
	v_lshl_add_u64 v[246:247], s[92:93], 0, v[0:1]
	s_mov_b32 m0, s61
	v_lshl_add_u64 v[248:249], s[52:53], 0, v[144:145]
	global_load_lds_dwordx4 v[246:247], off
	v_lshl_add_u64 v[246:247], s[92:93], 0, v[142:143]
	s_mov_b32 m0, s62
	s_nop 0
	global_load_lds_dwordx4 v[246:247], off
	v_lshl_add_u64 v[246:247], s[52:53], 0, v[148:149]
	s_mov_b32 m0, s58
	s_nop 0
	global_load_lds_dwordx4 v[246:247], off
	s_mov_b32 m0, s63
	s_nop 0
	global_load_lds_dwordx4 v[248:249], off
	s_waitcnt vmcnt(8)
	s_waitcnt lgkmcnt(0)
	s_barrier
	s_setprio 1
	s_waitcnt lgkmcnt(0)
	v_mfma_f32_16x16x32_bf16 v[62:65], v[164:167], v[200:203], v[62:65]
	v_mfma_f32_16x16x32_bf16 v[58:61], v[172:175], v[200:203], v[58:61]
	v_mfma_f32_16x16x32_bf16 v[54:57], v[164:167], v[208:211], v[54:57]
	v_mfma_f32_16x16x32_bf16 v[46:49], v[172:175], v[208:211], v[46:49]
	v_mfma_f32_16x16x32_bf16 v[30:33], v[164:167], v[216:219], v[30:33]
	v_mfma_f32_16x16x32_bf16 v[26:29], v[172:175], v[216:219], v[26:29]
	v_mfma_f32_16x16x32_bf16 v[22:25], v[164:167], v[236:239], v[22:25]
	v_mfma_f32_16x16x32_bf16 v[14:17], v[172:175], v[236:239], v[14:17]
	v_mfma_f32_16x16x32_bf16 v[62:65], v[168:171], v[204:207], v[62:65]
	v_mfma_f32_16x16x32_bf16 v[58:61], v[176:179], v[204:207], v[58:61]
	v_mfma_f32_16x16x32_bf16 v[54:57], v[168:171], v[212:215], v[54:57]
	v_mfma_f32_16x16x32_bf16 v[46:49], v[176:179], v[212:215], v[46:49]
	v_mfma_f32_16x16x32_bf16 v[30:33], v[168:171], v[220:223], v[30:33]
	v_mfma_f32_16x16x32_bf16 v[26:29], v[176:179], v[220:223], v[26:29]
	v_mfma_f32_16x16x32_bf16 v[22:25], v[168:171], v[240:243], v[22:25]
	v_mfma_f32_16x16x32_bf16 v[14:17], v[176:179], v[240:243], v[14:17]
	s_setprio 0
	s_setprio 1
	v_mfma_f32_16x16x32_bf16 v[50:53], v[180:183], v[200:203], v[50:53]
	v_mfma_f32_16x16x32_bf16 v[42:45], v[188:191], v[200:203], v[42:45]
	v_mfma_f32_16x16x32_bf16 v[38:41], v[180:183], v[208:211], v[38:41]
	v_mfma_f32_16x16x32_bf16 v[34:37], v[188:191], v[208:211], v[34:37]
	v_mfma_f32_16x16x32_bf16 v[18:21], v[180:183], v[216:219], v[18:21]
	v_mfma_f32_16x16x32_bf16 v[10:13], v[188:191], v[216:219], v[10:13]
	v_mfma_f32_16x16x32_bf16 v[6:9], v[180:183], v[236:239], v[6:9]
	v_mfma_f32_16x16x32_bf16 v[2:5], v[188:191], v[236:239], v[2:5]
	v_mfma_f32_16x16x32_bf16 v[50:53], v[184:187], v[204:207], v[50:53]
	v_mfma_f32_16x16x32_bf16 v[42:45], v[192:195], v[204:207], v[42:45]
	v_mfma_f32_16x16x32_bf16 v[38:41], v[184:187], v[212:215], v[38:41]
	v_mfma_f32_16x16x32_bf16 v[34:37], v[192:195], v[212:215], v[34:37]
	v_mfma_f32_16x16x32_bf16 v[18:21], v[184:187], v[220:223], v[18:21]
	v_mfma_f32_16x16x32_bf16 v[10:13], v[192:195], v[220:223], v[10:13]
	v_mfma_f32_16x16x32_bf16 v[6:9], v[184:187], v[240:243], v[6:9]
	v_mfma_f32_16x16x32_bf16 v[2:5], v[192:195], v[240:243], v[2:5]
	s_setprio 0
	s_barrier
	v_or_b32_e32 v163, 0x18000, v162
	v_add_u32_e32 v168, 0x18400, v162
	ds_read_b128 v[164:167], v163
	ds_read_b128 v[168:171], v168
	v_add_u32_e32 v163, 0x18800, v162
	v_add_u32_e32 v176, 0x18c00, v162
	ds_read_b128 v[172:175], v163
	ds_read_b128 v[176:179], v176
	v_or_b32_e32 v163, 0x1c000, v162
	v_add_u32_e32 v184, 0x1c400, v162
	ds_read_b128 v[180:183], v163
	ds_read_b128 v[184:187], v184
	v_add_u32_e32 v163, 0x1c800, v162
	v_add_u32_e32 v192, 0x1cc00, v162
	ds_read_b128 v[188:191], v163
	ds_read_b128 v[192:195], v192
	s_add_u32 s52, s52, 0x40000
	s_addc_u32 s53, s53, 0
	s_mov_b32 m0, s64
	v_lshl_add_u64 v[228:229], s[52:53], 0, v[148:149]
	ds_read_b128 v[200:203], v161 offset:32768
	ds_read_b128 v[204:207], v161 offset:33792
	ds_read_b128 v[208:211], v161 offset:34816
	ds_read_b128 v[212:215], v161 offset:35840
	ds_read_b128 v[216:219], v161 offset:36864
	ds_read_b128 v[220:223], v161 offset:37888
	ds_read_b128 v[236:239], v161 offset:38912
	ds_read_b128 v[240:243], v161 offset:39936
	global_load_lds_dwordx4 v[228:229], off
	v_lshl_add_u64 v[228:229], s[52:53], 0, v[144:145]
	s_mov_b32 m0, s65
	s_nop 0
	global_load_lds_dwordx4 v[228:229], off
	s_waitcnt vmcnt(8)
	s_waitcnt lgkmcnt(0)
	s_barrier
	s_setprio 1
	s_waitcnt lgkmcnt(0)
	v_mfma_f32_16x16x32_bf16 v[126:129], v[164:167], v[200:203], v[126:129]
	v_mfma_f32_16x16x32_bf16 v[122:125], v[172:175], v[200:203], v[122:125]
	v_mfma_f32_16x16x32_bf16 v[110:113], v[164:167], v[208:211], v[110:113]
	v_mfma_f32_16x16x32_bf16 v[106:109], v[172:175], v[208:211], v[106:109]
	v_mfma_f32_16x16x32_bf16 v[94:97], v[164:167], v[216:219], v[94:97]
	v_mfma_f32_16x16x32_bf16 v[90:93], v[172:175], v[216:219], v[90:93]
	v_mfma_f32_16x16x32_bf16 v[86:89], v[164:167], v[236:239], v[86:89]
	v_mfma_f32_16x16x32_bf16 v[78:81], v[172:175], v[236:239], v[78:81]
	v_mfma_f32_16x16x32_bf16 v[126:129], v[168:171], v[204:207], v[126:129]
	v_mfma_f32_16x16x32_bf16 v[122:125], v[176:179], v[204:207], v[122:125]
	v_mfma_f32_16x16x32_bf16 v[110:113], v[168:171], v[212:215], v[110:113]
	v_mfma_f32_16x16x32_bf16 v[106:109], v[176:179], v[212:215], v[106:109]
	v_mfma_f32_16x16x32_bf16 v[94:97], v[168:171], v[220:223], v[94:97]
	v_mfma_f32_16x16x32_bf16 v[90:93], v[176:179], v[220:223], v[90:93]
	v_mfma_f32_16x16x32_bf16 v[86:89], v[168:171], v[240:243], v[86:89]
	v_mfma_f32_16x16x32_bf16 v[78:81], v[176:179], v[240:243], v[78:81]
	s_setprio 0
	s_setprio 1
	v_mfma_f32_16x16x32_bf16 v[118:121], v[180:183], v[200:203], v[118:121]
	v_mfma_f32_16x16x32_bf16 v[114:117], v[188:191], v[200:203], v[114:117]
	v_mfma_f32_16x16x32_bf16 v[102:105], v[180:183], v[208:211], v[102:105]
	v_mfma_f32_16x16x32_bf16 v[98:101], v[188:191], v[208:211], v[98:101]
	v_mfma_f32_16x16x32_bf16 v[82:85], v[180:183], v[216:219], v[82:85]
	v_mfma_f32_16x16x32_bf16 v[74:77], v[188:191], v[216:219], v[74:77]
	v_mfma_f32_16x16x32_bf16 v[70:73], v[180:183], v[236:239], v[70:73]
	v_mfma_f32_16x16x32_bf16 v[66:69], v[188:191], v[236:239], v[66:69]
	v_mfma_f32_16x16x32_bf16 v[118:121], v[184:187], v[204:207], v[118:121]
	v_mfma_f32_16x16x32_bf16 v[114:117], v[192:195], v[204:207], v[114:117]
	v_mfma_f32_16x16x32_bf16 v[102:105], v[184:187], v[212:215], v[102:105]
	v_mfma_f32_16x16x32_bf16 v[98:101], v[192:195], v[212:215], v[98:101]
	v_mfma_f32_16x16x32_bf16 v[82:85], v[184:187], v[220:223], v[82:85]
	v_mfma_f32_16x16x32_bf16 v[74:77], v[192:195], v[220:223], v[74:77]
	v_mfma_f32_16x16x32_bf16 v[70:73], v[184:187], v[240:243], v[70:73]
	v_mfma_f32_16x16x32_bf16 v[66:69], v[192:195], v[240:243], v[66:69]
	s_setprio 0
	s_barrier
	s_mov_b32 m0, s66
	v_lshl_add_u64 v[226:227], v[226:227], 0, s[18:19]
	s_add_u32 s50, s50, 0x40080
	ds_read_b128 v[200:203], v161 offset:49152
	ds_read_b128 v[204:207], v161 offset:50176
	ds_read_b128 v[208:211], v161 offset:51200
	ds_read_b128 v[212:215], v161 offset:52224
	ds_read_b128 v[216:219], v161 offset:53248
	ds_read_b128 v[220:223], v161 offset:54272
	ds_read_b128 v[236:239], v161 offset:55296
	ds_read_b128 v[240:243], v161 offset:56320
	global_load_lds_dwordx4 v[226:227], off
	v_lshl_add_u64 v[226:227], v[244:245], 0, s[18:19]
	s_mov_b32 m0, s67
	s_addc_u32 s51, s51, 0
	global_load_lds_dwordx4 v[226:227], off
	v_lshl_add_u64 v[226:227], s[50:51], 0, v[0:1]
	s_mov_b32 m0, s83
	s_nop 0
	global_load_lds_dwordx4 v[226:227], off
	v_lshl_add_u64 v[226:227], s[50:51], 0, v[142:143]
	s_mov_b32 m0, s84
	s_nop 0
	global_load_lds_dwordx4 v[226:227], off
	v_lshl_add_u64 v[226:227], v[246:247], 0, s[18:19]
	s_mov_b32 m0, s80
	s_nop 0
	global_load_lds_dwordx4 v[226:227], off
	v_lshl_add_u64 v[226:227], v[248:249], 0, s[18:19]
	s_mov_b32 m0, s82
	s_nop 0
	global_load_lds_dwordx4 v[226:227], off
	s_waitcnt vmcnt(8)
	s_waitcnt lgkmcnt(0)
	s_barrier
	s_setprio 1
	s_waitcnt lgkmcnt(0)
	v_mfma_f32_16x16x32_bf16 v[62:65], v[164:167], v[200:203], v[62:65]
	v_mfma_f32_16x16x32_bf16 v[58:61], v[172:175], v[200:203], v[58:61]
	v_mfma_f32_16x16x32_bf16 v[54:57], v[164:167], v[208:211], v[54:57]
	v_mfma_f32_16x16x32_bf16 v[46:49], v[172:175], v[208:211], v[46:49]
	v_mfma_f32_16x16x32_bf16 v[30:33], v[164:167], v[216:219], v[30:33]
	v_mfma_f32_16x16x32_bf16 v[26:29], v[172:175], v[216:219], v[26:29]
	v_mfma_f32_16x16x32_bf16 v[22:25], v[164:167], v[236:239], v[22:25]
	v_mfma_f32_16x16x32_bf16 v[14:17], v[172:175], v[236:239], v[14:17]
	v_mfma_f32_16x16x32_bf16 v[62:65], v[168:171], v[204:207], v[62:65]
	v_mfma_f32_16x16x32_bf16 v[58:61], v[176:179], v[204:207], v[58:61]
	v_mfma_f32_16x16x32_bf16 v[54:57], v[168:171], v[212:215], v[54:57]
	v_mfma_f32_16x16x32_bf16 v[46:49], v[176:179], v[212:215], v[46:49]
	v_mfma_f32_16x16x32_bf16 v[30:33], v[168:171], v[220:223], v[30:33]
	v_mfma_f32_16x16x32_bf16 v[26:29], v[176:179], v[220:223], v[26:29]
	v_mfma_f32_16x16x32_bf16 v[22:25], v[168:171], v[240:243], v[22:25]
	v_mfma_f32_16x16x32_bf16 v[14:17], v[176:179], v[240:243], v[14:17]
	s_setprio 0
	s_setprio 1
	v_mfma_f32_16x16x32_bf16 v[50:53], v[180:183], v[200:203], v[50:53]
	v_mfma_f32_16x16x32_bf16 v[42:45], v[188:191], v[200:203], v[42:45]
	v_mfma_f32_16x16x32_bf16 v[38:41], v[180:183], v[208:211], v[38:41]
	v_mfma_f32_16x16x32_bf16 v[34:37], v[188:191], v[208:211], v[34:37]
	v_mfma_f32_16x16x32_bf16 v[18:21], v[180:183], v[216:219], v[18:21]
	v_mfma_f32_16x16x32_bf16 v[10:13], v[188:191], v[216:219], v[10:13]
	v_mfma_f32_16x16x32_bf16 v[6:9], v[180:183], v[236:239], v[6:9]
	v_mfma_f32_16x16x32_bf16 v[2:5], v[188:191], v[236:239], v[2:5]
	v_mfma_f32_16x16x32_bf16 v[50:53], v[184:187], v[204:207], v[50:53]
	v_mfma_f32_16x16x32_bf16 v[42:45], v[192:195], v[204:207], v[42:45]
	v_mfma_f32_16x16x32_bf16 v[38:41], v[184:187], v[212:215], v[38:41]
	v_mfma_f32_16x16x32_bf16 v[34:37], v[192:195], v[212:215], v[34:37]
	v_mfma_f32_16x16x32_bf16 v[18:21], v[184:187], v[220:223], v[18:21]
	v_mfma_f32_16x16x32_bf16 v[10:13], v[192:195], v[220:223], v[10:13]
	v_mfma_f32_16x16x32_bf16 v[6:9], v[184:187], v[240:243], v[6:9]
	v_mfma_f32_16x16x32_bf16 v[2:5], v[192:195], v[240:243], v[2:5]
	s_setprio 0
	s_barrier
	s_add_i32 s90, s90, 2
	s_add_u32 s48, s48, 0x100
	s_addc_u32 s49, s49, 0
	s_cmp_gt_u32 s90, 13
	s_cbranch_scc0 .LBB0_438
	s_add_u32 s48, s41, 0xffffff00
	s_addc_u32 s49, s89, -1
	s_and_b64 vcc, exec, s[36:37]
	s_movk_i32 s90, 0xfea0
	s_cbranch_vccnz .LBB0_441
	v_lshl_add_u32 v2, s38, 8, v160
	v_ashrrev_i32_e32 v3, 31, v2
	v_lshl_add_u64 v[2:3], v[2:3], 3, s[14:15]
	global_load_dwordx2 v[150:151], v[2:3], off nt
	global_load_dwordx2 v[146:147], v[2:3], off offset:128 nt
	global_load_dwordx2 v[140:141], v[2:3], off offset:256 nt
	global_load_dwordx2 v[138:139], v[2:3], off offset:384 nt
	global_load_dwordx2 v[136:137], v[2:3], off offset:1024 nt
	global_load_dwordx2 v[134:135], v[2:3], off offset:1152 nt
	global_load_dwordx2 v[132:133], v[2:3], off offset:1280 nt
	global_load_dwordx2 v[130:131], v[2:3], off offset:1408 nt
	v_mov_b32_e32 v2, 0
	s_mov_b32 s0, s40
	s_mov_b32 s34, s38
	s_mov_b64 s[16:17], s[46:47]
	s_mov_b32 s85, s88
	v_mov_b32_e32 v3, v2
	v_mov_b64_e32 v[4:5], v[2:3]
	v_mov_b64_e32 v[6:7], v[2:3]
	v_mov_b64_e32 v[8:9], v[2:3]
	v_mov_b64_e32 v[10:11], v[2:3]
	v_mov_b64_e32 v[12:13], v[2:3]
	v_mov_b64_e32 v[14:15], v[2:3]
	v_mov_b64_e32 v[16:17], v[2:3]
	v_mov_b64_e32 v[18:19], v[2:3]
	v_mov_b64_e32 v[20:21], v[2:3]
	v_mov_b64_e32 v[22:23], v[2:3]
	v_mov_b64_e32 v[24:25], v[2:3]
	v_mov_b64_e32 v[26:27], v[2:3]
	v_mov_b64_e32 v[28:29], v[2:3]
	v_mov_b64_e32 v[30:31], v[2:3]
	v_mov_b64_e32 v[32:33], v[2:3]
	v_mov_b64_e32 v[34:35], v[2:3]
	v_mov_b64_e32 v[36:37], v[2:3]
	v_mov_b64_e32 v[38:39], v[2:3]
	v_mov_b64_e32 v[40:41], v[2:3]
	v_mov_b64_e32 v[42:43], v[2:3]
	v_mov_b64_e32 v[44:45], v[2:3]
	v_mov_b64_e32 v[46:47], v[2:3]
	v_mov_b64_e32 v[48:49], v[2:3]
	v_mov_b64_e32 v[50:51], v[2:3]
	v_mov_b64_e32 v[52:53], v[2:3]
	v_mov_b64_e32 v[54:55], v[2:3]
	v_mov_b64_e32 v[56:57], v[2:3]
	v_mov_b64_e32 v[58:59], v[2:3]
	v_mov_b64_e32 v[60:61], v[2:3]
	v_mov_b64_e32 v[62:63], v[2:3]
	v_mov_b64_e32 v[64:65], v[2:3]
	v_mov_b64_e32 v[66:67], v[2:3]
	v_mov_b64_e32 v[68:69], v[2:3]
	v_mov_b64_e32 v[70:71], v[2:3]
	v_mov_b64_e32 v[72:73], v[2:3]
	v_mov_b64_e32 v[74:75], v[2:3]
	v_mov_b64_e32 v[76:77], v[2:3]
	v_mov_b64_e32 v[78:79], v[2:3]
	v_mov_b64_e32 v[80:81], v[2:3]
	v_mov_b64_e32 v[82:83], v[2:3]
	v_mov_b64_e32 v[84:85], v[2:3]
	v_mov_b64_e32 v[86:87], v[2:3]
	v_mov_b64_e32 v[88:89], v[2:3]
	v_mov_b64_e32 v[90:91], v[2:3]
	v_mov_b64_e32 v[92:93], v[2:3]
	v_mov_b64_e32 v[94:95], v[2:3]
	v_mov_b64_e32 v[96:97], v[2:3]
	v_mov_b64_e32 v[98:99], v[2:3]
	v_mov_b64_e32 v[100:101], v[2:3]
	v_mov_b64_e32 v[102:103], v[2:3]
	v_mov_b64_e32 v[104:105], v[2:3]
	v_mov_b64_e32 v[106:107], v[2:3]
	v_mov_b64_e32 v[108:109], v[2:3]
	v_mov_b64_e32 v[110:111], v[2:3]
	v_mov_b64_e32 v[112:113], v[2:3]
	v_mov_b64_e32 v[114:115], v[2:3]
	v_mov_b64_e32 v[116:117], v[2:3]
	v_mov_b64_e32 v[118:119], v[2:3]
	v_mov_b64_e32 v[120:121], v[2:3]
	v_mov_b64_e32 v[122:123], v[2:3]
	v_mov_b64_e32 v[124:125], v[2:3]
	v_mov_b64_e32 v[126:127], v[2:3]
	v_mov_b64_e32 v[128:129], v[2:3]
	s_branch .LBB0_442

.LBB0_502:
	v_mov_b32_e32 v2, 0
	s_mov_b32 s16, s40
	s_mov_b32 s90, s38
	v_mov_b32_e32 v3, v2
	v_mov_b64_e32 v[4:5], v[2:3]
	v_mov_b64_e32 v[6:7], v[2:3]
	v_mov_b64_e32 v[8:9], v[2:3]
	v_mov_b64_e32 v[10:11], v[2:3]
	v_mov_b64_e32 v[12:13], v[2:3]
	v_mov_b64_e32 v[14:15], v[2:3]
	v_mov_b64_e32 v[16:17], v[2:3]
	v_mov_b64_e32 v[18:19], v[2:3]
	v_mov_b64_e32 v[20:21], v[2:3]
	v_mov_b64_e32 v[22:23], v[2:3]
	v_mov_b64_e32 v[24:25], v[2:3]
	v_mov_b64_e32 v[26:27], v[2:3]
	v_mov_b64_e32 v[28:29], v[2:3]
	v_mov_b64_e32 v[30:31], v[2:3]
	v_mov_b64_e32 v[32:33], v[2:3]
	v_mov_b64_e32 v[34:35], v[2:3]
	v_mov_b64_e32 v[36:37], v[2:3]
	v_mov_b64_e32 v[38:39], v[2:3]
	v_mov_b64_e32 v[40:41], v[2:3]
	v_mov_b64_e32 v[42:43], v[2:3]
	v_mov_b64_e32 v[44:45], v[2:3]
	v_mov_b64_e32 v[46:47], v[2:3]
	v_mov_b64_e32 v[48:49], v[2:3]
	v_mov_b64_e32 v[50:51], v[2:3]
	v_mov_b64_e32 v[52:53], v[2:3]
	v_mov_b64_e32 v[54:55], v[2:3]
	v_mov_b64_e32 v[56:57], v[2:3]
	v_mov_b64_e32 v[58:59], v[2:3]
	v_mov_b64_e32 v[60:61], v[2:3]
	v_mov_b64_e32 v[62:63], v[2:3]
	v_mov_b64_e32 v[64:65], v[2:3]
	v_mov_b64_e32 v[66:67], v[2:3]
	v_mov_b64_e32 v[68:69], v[2:3]
	v_mov_b64_e32 v[70:71], v[2:3]
	v_mov_b64_e32 v[72:73], v[2:3]
	v_mov_b64_e32 v[74:75], v[2:3]
	v_mov_b64_e32 v[76:77], v[2:3]
	v_mov_b64_e32 v[78:79], v[2:3]
	v_mov_b64_e32 v[80:81], v[2:3]
	v_mov_b64_e32 v[82:83], v[2:3]
	v_mov_b64_e32 v[84:85], v[2:3]
	v_mov_b64_e32 v[86:87], v[2:3]
	v_mov_b64_e32 v[88:89], v[2:3]
	v_mov_b64_e32 v[90:91], v[2:3]
	v_mov_b64_e32 v[92:93], v[2:3]
	v_mov_b64_e32 v[94:95], v[2:3]
	v_mov_b64_e32 v[96:97], v[2:3]
	v_mov_b64_e32 v[98:99], v[2:3]
	v_mov_b64_e32 v[100:101], v[2:3]
	v_mov_b64_e32 v[102:103], v[2:3]
	v_mov_b64_e32 v[104:105], v[2:3]
	v_mov_b64_e32 v[106:107], v[2:3]
	v_mov_b64_e32 v[108:109], v[2:3]
	v_mov_b64_e32 v[110:111], v[2:3]
	v_mov_b64_e32 v[112:113], v[2:3]
	v_mov_b64_e32 v[114:115], v[2:3]
	v_mov_b64_e32 v[116:117], v[2:3]
	v_mov_b64_e32 v[118:119], v[2:3]
	v_mov_b64_e32 v[120:121], v[2:3]
	v_mov_b64_e32 v[122:123], v[2:3]
	v_mov_b64_e32 v[124:125], v[2:3]
	v_mov_b64_e32 v[126:127], v[2:3]
	v_mov_b64_e32 v[128:129], v[2:3]
	s_andn2_b64 vcc, exec, s[42:43]
	s_cbranch_vccnz .LBB0_488

.LBB0_527:
	v_lshl_add_u64 v[10:11], s[52:53], 0, v[0:1]
	v_mov_b32_e32 v131, v1
	v_and_b32_e32 v9, 48, v4
	v_lshlrev_b32_e32 v18, 6, v4
	s_movk_i32 s1, 0x3c0
	v_lshlrev_b32_e32 v4, 2, v4
	s_add_i32 s82, s37, 0x18000
	v_lshl_add_u64 v[12:13], s[52:53], 0, v[130:131]
	v_mov_b32_e32 v135, v1
	s_and_b32 s61, s17, 3
	s_lshl_b32 s0, s16, 13
	v_and_or_b32 v9, v18, s1, v9
	v_and_b32_e32 v4, 32, v4
	v_lshl_add_u64 v[10:11], v[10:11], 0, s[18:19]
	s_mov_b32 m0, s82
	s_add_i32 s83, s37, 0x1a000
	v_lshl_add_u64 v[14:15], s[42:43], 0, v[134:135]
	v_mov_b32_e32 v133, v1
	s_lshl_b32 s60, s16, 6
	v_bitop3_b32 v144, v9, s0, v4 bitop3:0xde
	s_lshl_b32 s0, s61, 12
	s_waitcnt vmcnt(2)
	s_barrier
	global_load_lds_dwordx4 v[10:11], off
	v_lshl_add_u64 v[10:11], v[12:13], 0, s[18:19]
	s_mov_b32 m0, s83
	s_add_i32 s84, s37, 0x8000
	s_add_i32 s85, s37, 0xa000
	v_lshl_add_u64 v[16:17], s[42:43], 0, v[132:133]
	global_load_lds_dwordx4 v[10:11], off
	v_lshl_add_u64 v[10:11], v[14:15], 0, s[18:19]
	s_mov_b32 m0, s84
	s_add_u32 s16, s52, 0x40080
	global_load_lds_dwordx4 v[10:11], off
	v_lshl_add_u64 v[10:11], v[16:17], 0, s[18:19]
	s_mov_b32 m0, s85
	s_addc_u32 s17, s53, 0
	s_add_i32 s88, s37, 0x1c000
	global_load_lds_dwordx4 v[10:11], off
	v_lshl_add_u64 v[10:11], s[16:17], 0, v[0:1]
	s_mov_b32 m0, s88
	s_add_i32 s89, s37, 0x1e000
	global_load_lds_dwordx4 v[10:11], off
	v_lshl_add_u64 v[10:11], s[16:17], 0, v[130:131]
	s_mov_b32 m0, s89
	v_bitop3_b32 v145, v9, s0, v4 bitop3:0xde
	global_load_lds_dwordx4 v[10:11], off
	v_lshlrev_b32_e32 v4, 14, v7
	v_and_b32_e32 v4, 0xffff8000, v4
	v_lshl_add_u32 v4, v6, 11, v4
	v_and_b32_e32 v6, 1, v7
	v_lshl_or_b32 v4, v6, 6, v4
	v_lshl_add_u32 v136, v8, 1, v4
	v_lshlrev_b32_e32 v4, 14, v2
	v_and_b32_e32 v4, 0xffff8000, v4
	v_lshl_add_u32 v3, v3, 11, v4
	v_and_b32_e32 v2, 1, v2
	v_readlane_b32 s0, v252, 7
	s_waitcnt vmcnt(6)
	v_lshl_or_b32 v2, v2, 6, v3
	v_readlane_b32 s1, v252, 8
	s_cmpk_lt_u32 s59, 0x100
	v_lshl_add_u32 v138, v5, 1, v2
	v_mov_b32_e32 v2, 0
	s_mov_b32 s36, s0
	v_readlane_b32 s0, v252, 3
	s_cselect_b64 s[16:17], -1, 0
	v_mov_b32_e32 v137, v1
	v_mov_b32_e32 v139, v1
	s_mov_b32 s92, 0
	s_mov_b32 s90, s0
	v_mov_b32_e32 v3, v2
	v_mov_b64_e32 v[4:5], v[2:3]
	v_mov_b64_e32 v[6:7], v[2:3]
	v_mov_b64_e32 v[8:9], v[2:3]
	v_mov_b64_e32 v[10:11], v[2:3]
	v_mov_b64_e32 v[12:13], v[2:3]
	v_mov_b64_e32 v[14:15], v[2:3]
	v_mov_b64_e32 v[16:17], v[2:3]
	v_mov_b64_e32 v[18:19], v[2:3]
	v_mov_b64_e32 v[20:21], v[2:3]
	v_mov_b64_e32 v[22:23], v[2:3]
	v_mov_b64_e32 v[24:25], v[2:3]
	v_mov_b64_e32 v[26:27], v[2:3]
	v_mov_b64_e32 v[28:29], v[2:3]
	v_mov_b64_e32 v[30:31], v[2:3]
	v_mov_b64_e32 v[32:33], v[2:3]
	v_mov_b64_e32 v[34:35], v[2:3]
	v_mov_b64_e32 v[36:37], v[2:3]
	v_mov_b64_e32 v[38:39], v[2:3]
	v_mov_b64_e32 v[40:41], v[2:3]
	v_mov_b64_e32 v[42:43], v[2:3]
	v_mov_b64_e32 v[44:45], v[2:3]
	v_mov_b64_e32 v[46:47], v[2:3]
	v_mov_b64_e32 v[48:49], v[2:3]
	v_mov_b64_e32 v[50:51], v[2:3]
	v_mov_b64_e32 v[52:53], v[2:3]
	v_mov_b64_e32 v[54:55], v[2:3]
	v_mov_b64_e32 v[56:57], v[2:3]
	v_mov_b64_e32 v[58:59], v[2:3]
	v_mov_b64_e32 v[60:61], v[2:3]
	v_mov_b64_e32 v[62:63], v[2:3]
	v_mov_b64_e32 v[64:65], v[2:3]
	v_mov_b64_e32 v[66:67], v[2:3]
	v_mov_b64_e32 v[68:69], v[2:3]
	v_mov_b64_e32 v[70:71], v[2:3]
	v_mov_b64_e32 v[72:73], v[2:3]
	v_mov_b64_e32 v[74:75], v[2:3]
	v_mov_b64_e32 v[76:77], v[2:3]
	v_mov_b64_e32 v[78:79], v[2:3]
	v_mov_b64_e32 v[80:81], v[2:3]
	v_mov_b64_e32 v[82:83], v[2:3]
	v_mov_b64_e32 v[84:85], v[2:3]
	v_mov_b64_e32 v[86:87], v[2:3]
	v_mov_b64_e32 v[88:89], v[2:3]
	v_mov_b64_e32 v[90:91], v[2:3]
	v_mov_b64_e32 v[92:93], v[2:3]
	v_mov_b64_e32 v[94:95], v[2:3]
	v_mov_b64_e32 v[96:97], v[2:3]
	v_mov_b64_e32 v[98:99], v[2:3]
	v_mov_b64_e32 v[100:101], v[2:3]
	v_mov_b64_e32 v[102:103], v[2:3]
	v_mov_b64_e32 v[104:105], v[2:3]
	v_mov_b64_e32 v[106:107], v[2:3]
	v_mov_b64_e32 v[108:109], v[2:3]
	v_mov_b64_e32 v[110:111], v[2:3]
	v_mov_b64_e32 v[112:113], v[2:3]
	v_mov_b64_e32 v[114:115], v[2:3]
	v_mov_b64_e32 v[116:117], v[2:3]
	v_mov_b64_e32 v[118:119], v[2:3]
	v_mov_b64_e32 v[120:121], v[2:3]
	v_mov_b64_e32 v[122:123], v[2:3]
	v_mov_b64_e32 v[124:125], v[2:3]
	v_mov_b64_e32 v[126:127], v[2:3]
	v_mov_b64_e32 v[128:129], v[2:3]
	s_barrier
	v_readlane_b32 s1, v252, 4

.LBB0_541:
	v_mov_b32_e32 v2, 0
	s_mov_b32 s36, s40
	s_mov_b32 s90, s38
	v_mov_b32_e32 v3, v2
	v_mov_b64_e32 v[4:5], v[2:3]
	v_mov_b64_e32 v[6:7], v[2:3]
	v_mov_b64_e32 v[8:9], v[2:3]
	v_mov_b64_e32 v[10:11], v[2:3]
	v_mov_b64_e32 v[12:13], v[2:3]
	v_mov_b64_e32 v[14:15], v[2:3]
	v_mov_b64_e32 v[16:17], v[2:3]
	v_mov_b64_e32 v[18:19], v[2:3]
	v_mov_b64_e32 v[20:21], v[2:3]
	v_mov_b64_e32 v[22:23], v[2:3]
	v_mov_b64_e32 v[24:25], v[2:3]
	v_mov_b64_e32 v[26:27], v[2:3]
	v_mov_b64_e32 v[28:29], v[2:3]
	v_mov_b64_e32 v[30:31], v[2:3]
	v_mov_b64_e32 v[32:33], v[2:3]
	v_mov_b64_e32 v[34:35], v[2:3]
	v_mov_b64_e32 v[36:37], v[2:3]
	v_mov_b64_e32 v[38:39], v[2:3]
	v_mov_b64_e32 v[40:41], v[2:3]
	v_mov_b64_e32 v[42:43], v[2:3]
	v_mov_b64_e32 v[44:45], v[2:3]
	v_mov_b64_e32 v[46:47], v[2:3]
	v_mov_b64_e32 v[48:49], v[2:3]
	v_mov_b64_e32 v[50:51], v[2:3]
	v_mov_b64_e32 v[52:53], v[2:3]
	v_mov_b64_e32 v[54:55], v[2:3]
	v_mov_b64_e32 v[56:57], v[2:3]
	v_mov_b64_e32 v[58:59], v[2:3]
	v_mov_b64_e32 v[60:61], v[2:3]
	v_mov_b64_e32 v[62:63], v[2:3]
	v_mov_b64_e32 v[64:65], v[2:3]
	v_mov_b64_e32 v[66:67], v[2:3]
	v_mov_b64_e32 v[68:69], v[2:3]
	v_mov_b64_e32 v[70:71], v[2:3]
	v_mov_b64_e32 v[72:73], v[2:3]
	v_mov_b64_e32 v[74:75], v[2:3]
	v_mov_b64_e32 v[76:77], v[2:3]
	v_mov_b64_e32 v[78:79], v[2:3]
	v_mov_b64_e32 v[80:81], v[2:3]
	v_mov_b64_e32 v[82:83], v[2:3]
	v_mov_b64_e32 v[84:85], v[2:3]
	v_mov_b64_e32 v[86:87], v[2:3]
	v_mov_b64_e32 v[88:89], v[2:3]
	v_mov_b64_e32 v[90:91], v[2:3]
	v_mov_b64_e32 v[92:93], v[2:3]
	v_mov_b64_e32 v[94:95], v[2:3]
	v_mov_b64_e32 v[96:97], v[2:3]
	v_mov_b64_e32 v[98:99], v[2:3]
	v_mov_b64_e32 v[100:101], v[2:3]
	v_mov_b64_e32 v[102:103], v[2:3]
	v_mov_b64_e32 v[104:105], v[2:3]
	v_mov_b64_e32 v[106:107], v[2:3]
	v_mov_b64_e32 v[108:109], v[2:3]
	v_mov_b64_e32 v[110:111], v[2:3]
	v_mov_b64_e32 v[112:113], v[2:3]
	v_mov_b64_e32 v[114:115], v[2:3]
	v_mov_b64_e32 v[116:117], v[2:3]
	v_mov_b64_e32 v[118:119], v[2:3]
	v_mov_b64_e32 v[120:121], v[2:3]
	v_mov_b64_e32 v[122:123], v[2:3]
	v_mov_b64_e32 v[124:125], v[2:3]
	v_mov_b64_e32 v[126:127], v[2:3]
	v_mov_b64_e32 v[128:129], v[2:3]
	s_branch .LBB0_543

.LBB0_575:
	s_add_u32 s14, s74, 0x2200000
	s_addc_u32 s15, s75, 0
	s_add_u32 s83, s74, 0x8800000
	v_and_b32_e32 v16, 48, v2
	v_lshlrev_b32_e32 v17, 6, v2
	s_movk_i32 s36, 0x3c0
	v_lshlrev_b32_e32 v2, 2, v2
	v_mov_b32_e32 v201, v1
	s_addc_u32 s84, s75, 0
	s_lshl_b32 s85, s17, 6
	s_lshl_b32 s17, s17, 13
	v_and_or_b32 v16, v17, s36, v16
	v_and_b32_e32 v2, 32, v2
	v_lshl_add_u64 v[8:9], s[56:57], 0, v[200:201]
	v_mov_b32_e32 v205, v1
	v_bitop3_b32 v236, v16, s17, v2 bitop3:0xde
	s_lshl_b32 s17, s29, 5
	s_add_i32 s88, s61, 0x18000
	v_lshl_add_u64 v[10:11], s[56:57], 0, v[204:205]
	v_mov_b32_e32 v195, v1
	s_and_b32 s80, s17, 0x60
	v_lshl_add_u64 v[8:9], v[8:9], 0, s[18:19]
	s_mov_b32 m0, s88
	s_add_i32 s89, s61, 0x1a000
	v_lshl_add_u64 v[12:13], s[54:55], 0, v[194:195]
	v_mov_b32_e32 v203, v1
	s_lshl_b32 s17, s80, 7
	s_waitcnt vmcnt(2)
	s_barrier
	global_load_lds_dwordx4 v[8:9], off
	v_lshl_add_u64 v[8:9], v[10:11], 0, s[18:19]
	s_mov_b32 m0, s89
	s_add_i32 s90, s61, 0x8000
	s_add_i32 s91, s61, 0xa000
	v_lshl_add_u64 v[14:15], s[54:55], 0, v[202:203]
	global_load_lds_dwordx4 v[8:9], off
	v_lshl_add_u64 v[8:9], v[12:13], 0, s[18:19]
	s_mov_b32 m0, s90
	s_add_u32 s36, s56, 0x20080
	global_load_lds_dwordx4 v[8:9], off
	v_lshl_add_u64 v[8:9], v[14:15], 0, s[18:19]
	s_mov_b32 m0, s91
	s_addc_u32 s37, s57, 0
	s_add_i32 s92, s61, 0x1c000
	global_load_lds_dwordx4 v[8:9], off
	v_lshl_add_u64 v[8:9], s[36:37], 0, v[200:201]
	s_mov_b32 m0, s92
	s_add_i32 s93, s61, 0x1e000
	global_load_lds_dwordx4 v[8:9], off
	v_lshl_add_u64 v[8:9], s[36:37], 0, v[204:205]
	s_mov_b32 m0, s93
	v_bitop3_b32 v237, s17, v16, v2 bitop3:0xf6
	global_load_lds_dwordx4 v[8:9], off
	v_lshlrev_b32_e32 v2, 13, v0
	v_and_b32_e32 v2, 0xffffc000, v2
	v_lshl_add_u32 v2, v3, 10, v2
	v_and_b32_e32 v0, 1, v0
	v_lshl_or_b32 v0, v0, 6, v2
	v_lshl_add_u32 v206, v4, 1, v0
	v_lshlrev_b32_e32 v0, 13, v5
	v_and_b32_e32 v0, 0xffffc000, v0
	s_waitcnt vmcnt(6)
	v_lshl_add_u32 v0, v6, 10, v0
	v_and_b32_e32 v2, 1, v5
	s_cmpk_lt_u32 s16, 0x100
	v_lshl_or_b32 v0, v2, 6, v0
	v_mov_b32_e32 v2, 0
	s_cselect_b64 s[16:17], -1, 0
	v_mov_b32_e32 v207, v1
	v_lshl_add_u32 v208, v7, 1, v0
	v_mov_b32_e32 v209, v1
	s_mov_b32 s94, 0
	v_readlane_b32 s52, v251, 51
	v_mov_b32_e32 v3, v2
	v_mov_b64_e32 v[4:5], v[2:3]
	v_mov_b64_e32 v[6:7], v[2:3]
	v_mov_b64_e32 v[8:9], v[2:3]
	v_mov_b64_e32 v[10:11], v[2:3]
	v_mov_b64_e32 v[12:13], v[2:3]
	v_mov_b64_e32 v[14:15], v[2:3]
	v_mov_b64_e32 v[16:17], v[2:3]
	v_mov_b64_e32 v[18:19], v[2:3]
	v_mov_b64_e32 v[20:21], v[2:3]
	v_mov_b64_e32 v[22:23], v[2:3]
	v_mov_b64_e32 v[24:25], v[2:3]
	v_mov_b64_e32 v[26:27], v[2:3]
	v_mov_b64_e32 v[28:29], v[2:3]
	v_mov_b64_e32 v[30:31], v[2:3]
	v_mov_b64_e32 v[32:33], v[2:3]
	v_mov_b64_e32 v[34:35], v[2:3]
	v_mov_b64_e32 v[36:37], v[2:3]
	v_mov_b64_e32 v[38:39], v[2:3]
	v_mov_b64_e32 v[40:41], v[2:3]
	v_mov_b64_e32 v[42:43], v[2:3]
	v_mov_b64_e32 v[44:45], v[2:3]
	v_mov_b64_e32 v[46:47], v[2:3]
	v_mov_b64_e32 v[48:49], v[2:3]
	v_mov_b64_e32 v[50:51], v[2:3]
	v_mov_b64_e32 v[52:53], v[2:3]
	v_mov_b64_e32 v[54:55], v[2:3]
	v_mov_b64_e32 v[56:57], v[2:3]
	v_mov_b64_e32 v[58:59], v[2:3]
	v_mov_b64_e32 v[60:61], v[2:3]
	v_mov_b64_e32 v[62:63], v[2:3]
	v_mov_b64_e32 v[64:65], v[2:3]
	v_mov_b64_e32 v[66:67], v[2:3]
	v_mov_b64_e32 v[68:69], v[2:3]
	v_mov_b64_e32 v[70:71], v[2:3]
	v_mov_b64_e32 v[72:73], v[2:3]
	v_mov_b64_e32 v[74:75], v[2:3]
	v_mov_b64_e32 v[76:77], v[2:3]
	v_mov_b64_e32 v[78:79], v[2:3]
	v_mov_b64_e32 v[80:81], v[2:3]
	v_mov_b64_e32 v[82:83], v[2:3]
	v_mov_b64_e32 v[84:85], v[2:3]
	v_mov_b64_e32 v[86:87], v[2:3]
	v_mov_b64_e32 v[88:89], v[2:3]
	v_mov_b64_e32 v[90:91], v[2:3]
	v_mov_b64_e32 v[92:93], v[2:3]
	v_mov_b64_e32 v[94:95], v[2:3]
	v_mov_b64_e32 v[96:97], v[2:3]
	v_mov_b64_e32 v[98:99], v[2:3]
	v_mov_b64_e32 v[100:101], v[2:3]
	v_mov_b64_e32 v[102:103], v[2:3]
	v_mov_b64_e32 v[104:105], v[2:3]
	v_mov_b64_e32 v[106:107], v[2:3]
	v_mov_b64_e32 v[108:109], v[2:3]
	v_mov_b64_e32 v[110:111], v[2:3]
	v_mov_b64_e32 v[112:113], v[2:3]
	v_mov_b64_e32 v[114:115], v[2:3]
	v_mov_b64_e32 v[116:117], v[2:3]
	v_mov_b64_e32 v[118:119], v[2:3]
	v_mov_b64_e32 v[120:121], v[2:3]
	v_mov_b64_e32 v[122:123], v[2:3]
	v_mov_b64_e32 v[124:125], v[2:3]
	v_mov_b64_e32 v[126:127], v[2:3]
	v_mov_b64_e32 v[128:129], v[2:3]
	s_barrier
	v_readlane_b32 s53, v251, 52
	s_branch .LBB0_840

.LBB0_953:
	v_mov_b32_e32 v2, 0
	v_mov_b32_e32 v3, v2
	v_mov_b64_e32 v[4:5], v[2:3]
	v_mov_b64_e32 v[6:7], v[2:3]
	v_mov_b64_e32 v[8:9], v[2:3]
	v_mov_b64_e32 v[10:11], v[2:3]
	v_mov_b64_e32 v[12:13], v[2:3]
	v_mov_b64_e32 v[14:15], v[2:3]
	v_mov_b64_e32 v[16:17], v[2:3]
	v_mov_b64_e32 v[18:19], v[2:3]
	v_mov_b64_e32 v[20:21], v[2:3]
	v_mov_b64_e32 v[22:23], v[2:3]
	v_mov_b64_e32 v[24:25], v[2:3]
	v_mov_b64_e32 v[26:27], v[2:3]
	v_mov_b64_e32 v[28:29], v[2:3]
	v_mov_b64_e32 v[30:31], v[2:3]
	v_mov_b64_e32 v[32:33], v[2:3]
	v_mov_b64_e32 v[34:35], v[2:3]
	v_mov_b64_e32 v[36:37], v[2:3]
	v_mov_b64_e32 v[38:39], v[2:3]
	v_mov_b64_e32 v[40:41], v[2:3]
	v_mov_b64_e32 v[42:43], v[2:3]
	v_mov_b64_e32 v[44:45], v[2:3]
	v_mov_b64_e32 v[46:47], v[2:3]
	v_mov_b64_e32 v[48:49], v[2:3]
	v_mov_b64_e32 v[50:51], v[2:3]
	v_mov_b64_e32 v[52:53], v[2:3]
	v_mov_b64_e32 v[54:55], v[2:3]
	v_mov_b64_e32 v[56:57], v[2:3]
	v_mov_b64_e32 v[58:59], v[2:3]
	v_mov_b64_e32 v[60:61], v[2:3]
	v_mov_b64_e32 v[62:63], v[2:3]
	v_mov_b64_e32 v[64:65], v[2:3]
	v_mov_b64_e32 v[66:67], v[2:3]
	v_mov_b64_e32 v[68:69], v[2:3]
	v_mov_b64_e32 v[70:71], v[2:3]
	v_mov_b64_e32 v[72:73], v[2:3]
	v_mov_b64_e32 v[74:75], v[2:3]
	v_mov_b64_e32 v[76:77], v[2:3]
	v_mov_b64_e32 v[78:79], v[2:3]
	v_mov_b64_e32 v[80:81], v[2:3]
	v_mov_b64_e32 v[82:83], v[2:3]
	v_mov_b64_e32 v[84:85], v[2:3]
	v_mov_b64_e32 v[86:87], v[2:3]
	v_mov_b64_e32 v[88:89], v[2:3]
	v_mov_b64_e32 v[90:91], v[2:3]
	v_mov_b64_e32 v[92:93], v[2:3]
	v_mov_b64_e32 v[94:95], v[2:3]
	v_mov_b64_e32 v[96:97], v[2:3]
	v_mov_b64_e32 v[98:99], v[2:3]
	v_mov_b64_e32 v[100:101], v[2:3]
	v_mov_b64_e32 v[102:103], v[2:3]
	v_mov_b64_e32 v[104:105], v[2:3]
	v_mov_b64_e32 v[106:107], v[2:3]
	v_mov_b64_e32 v[108:109], v[2:3]
	v_mov_b64_e32 v[110:111], v[2:3]
	v_mov_b64_e32 v[112:113], v[2:3]
	v_mov_b64_e32 v[114:115], v[2:3]
	v_mov_b64_e32 v[116:117], v[2:3]
	v_mov_b64_e32 v[118:119], v[2:3]
	v_mov_b64_e32 v[120:121], v[2:3]
	v_mov_b64_e32 v[122:123], v[2:3]
	v_mov_b64_e32 v[124:125], v[2:3]
	v_mov_b64_e32 v[126:127], v[2:3]
	v_mov_b64_e32 v[128:129], v[2:3]
	s_andn2_b64 vcc, exec, s[0:1]
	s_cbranch_vccnz .LBB0_838

.LBB0_1057:
	s_ashr_i32 s39, s38, 31
	s_lshl_b64 s[42:43], s[38:39], 19
	v_readlane_b32 s44, v253, 34
	v_readlane_b32 s45, v253, 35
	s_add_u32 s42, s44, s42
	s_addc_u32 s43, s45, s43
	s_and_b64 s[44:45], s[46:47], exec
	s_cselect_b32 s29, s43, s37
	s_cselect_b32 s39, s42, s36
	s_ashr_i32 s41, s40, 31
	s_lshl_b64 s[44:45], s[40:41], 19
	s_add_u32 s44, s31, s44
	s_addc_u32 s45, s34, s45
	s_and_b64 s[50:51], s[46:47], exec
	s_cselect_b32 s41, s45, s49
	s_cselect_b32 s85, s44, s48
	s_add_u32 s36, s36, 0x40080
	s_addc_u32 s37, s37, 0
	s_add_u32 s88, s48, 0x100
	v_mov_b32_e32 v2, 0
	s_addc_u32 s89, s49, 0
	s_mov_b32 s90, -2
	v_mov_b32_e32 v3, v2
	v_mov_b64_e32 v[4:5], v[2:3]
	v_mov_b64_e32 v[6:7], v[2:3]
	v_mov_b64_e32 v[8:9], v[2:3]
	v_mov_b64_e32 v[10:11], v[2:3]
	v_mov_b64_e32 v[12:13], v[2:3]
	v_mov_b64_e32 v[14:15], v[2:3]
	v_mov_b64_e32 v[16:17], v[2:3]
	v_mov_b64_e32 v[18:19], v[2:3]
	v_mov_b64_e32 v[20:21], v[2:3]
	v_mov_b64_e32 v[22:23], v[2:3]
	v_mov_b64_e32 v[24:25], v[2:3]
	v_mov_b64_e32 v[26:27], v[2:3]
	v_mov_b64_e32 v[28:29], v[2:3]
	v_mov_b64_e32 v[30:31], v[2:3]
	v_mov_b64_e32 v[32:33], v[2:3]
	v_mov_b64_e32 v[34:35], v[2:3]
	v_mov_b64_e32 v[36:37], v[2:3]
	v_mov_b64_e32 v[38:39], v[2:3]
	v_mov_b64_e32 v[40:41], v[2:3]
	v_mov_b64_e32 v[42:43], v[2:3]
	v_mov_b64_e32 v[44:45], v[2:3]
	v_mov_b64_e32 v[46:47], v[2:3]
	v_mov_b64_e32 v[48:49], v[2:3]
	v_mov_b64_e32 v[50:51], v[2:3]
	v_mov_b64_e32 v[52:53], v[2:3]
	v_mov_b64_e32 v[54:55], v[2:3]
	v_mov_b64_e32 v[56:57], v[2:3]
	v_mov_b64_e32 v[58:59], v[2:3]
	v_mov_b64_e32 v[60:61], v[2:3]
	v_mov_b64_e32 v[62:63], v[2:3]
	v_mov_b64_e32 v[64:65], v[2:3]
	v_mov_b64_e32 v[66:67], v[2:3]
	v_mov_b64_e32 v[68:69], v[2:3]
	v_mov_b64_e32 v[70:71], v[2:3]
	v_mov_b64_e32 v[72:73], v[2:3]
	v_mov_b64_e32 v[74:75], v[2:3]
	v_mov_b64_e32 v[76:77], v[2:3]
	v_mov_b64_e32 v[78:79], v[2:3]
	v_mov_b64_e32 v[80:81], v[2:3]
	v_mov_b64_e32 v[82:83], v[2:3]
	v_mov_b64_e32 v[84:85], v[2:3]
	v_mov_b64_e32 v[86:87], v[2:3]
	v_mov_b64_e32 v[88:89], v[2:3]
	v_mov_b64_e32 v[90:91], v[2:3]
	v_mov_b64_e32 v[92:93], v[2:3]
	v_mov_b64_e32 v[94:95], v[2:3]
	v_mov_b64_e32 v[96:97], v[2:3]
	v_mov_b64_e32 v[98:99], v[2:3]
	v_mov_b64_e32 v[100:101], v[2:3]
	v_mov_b64_e32 v[102:103], v[2:3]
	v_mov_b64_e32 v[104:105], v[2:3]
	v_mov_b64_e32 v[106:107], v[2:3]
	v_mov_b64_e32 v[108:109], v[2:3]
	v_mov_b64_e32 v[110:111], v[2:3]
	v_mov_b64_e32 v[112:113], v[2:3]
	v_mov_b64_e32 v[114:115], v[2:3]
	v_mov_b64_e32 v[116:117], v[2:3]
	v_mov_b64_e32 v[118:119], v[2:3]
	v_mov_b64_e32 v[120:121], v[2:3]
	v_mov_b64_e32 v[122:123], v[2:3]
	v_mov_b64_e32 v[124:125], v[2:3]
	v_mov_b64_e32 v[126:127], v[2:3]
	v_mov_b64_e32 v[128:129], v[2:3]

.LBB0_1194:
	s_ashr_i32 s40, s62, 2
	s_ashr_i32 s41, s40, 31
	s_lshl_b64 s[40:41], s[40:41], 20
	s_add_u32 s17, s31, s40
	s_addc_u32 s41, s34, s41
	s_add_u32 s40, s17, s29
	s_addc_u32 s41, s41, 0
	s_and_b64 s[48:49], s[48:49], exec
	v_mov_b32_e32 v2, 0
	s_cselect_b32 s17, s41, s45
	s_cselect_b32 s29, s40, s44
	s_mov_b64 s[52:53], 0
	s_mov_b64 s[48:49], -1
	s_mov_b64 s[50:51], 0
	v_mov_b32_e32 v3, v2
	v_mov_b64_e32 v[4:5], v[2:3]
	v_mov_b64_e32 v[6:7], v[2:3]
	v_mov_b64_e32 v[8:9], v[2:3]
	v_mov_b64_e32 v[10:11], v[2:3]
	v_mov_b64_e32 v[12:13], v[2:3]
	v_mov_b64_e32 v[14:15], v[2:3]
	v_mov_b64_e32 v[16:17], v[2:3]
	v_mov_b64_e32 v[18:19], v[2:3]
	v_mov_b64_e32 v[20:21], v[2:3]
	v_mov_b64_e32 v[22:23], v[2:3]
	v_mov_b64_e32 v[24:25], v[2:3]
	v_mov_b64_e32 v[26:27], v[2:3]
	v_mov_b64_e32 v[28:29], v[2:3]
	v_mov_b64_e32 v[30:31], v[2:3]
	v_mov_b64_e32 v[32:33], v[2:3]
	v_mov_b64_e32 v[34:35], v[2:3]
	v_mov_b64_e32 v[36:37], v[2:3]
	v_mov_b64_e32 v[38:39], v[2:3]
	v_mov_b64_e32 v[40:41], v[2:3]
	v_mov_b64_e32 v[42:43], v[2:3]
	v_mov_b64_e32 v[44:45], v[2:3]
	v_mov_b64_e32 v[46:47], v[2:3]
	v_mov_b64_e32 v[48:49], v[2:3]
	v_mov_b64_e32 v[50:51], v[2:3]
	v_mov_b64_e32 v[52:53], v[2:3]
	v_mov_b64_e32 v[54:55], v[2:3]
	v_mov_b64_e32 v[56:57], v[2:3]
	v_mov_b64_e32 v[58:59], v[2:3]
	v_mov_b64_e32 v[60:61], v[2:3]
	v_mov_b64_e32 v[62:63], v[2:3]
	v_mov_b64_e32 v[64:65], v[2:3]
	v_mov_b64_e32 v[66:67], v[2:3]
	v_mov_b64_e32 v[68:69], v[2:3]
	v_mov_b64_e32 v[70:71], v[2:3]
	v_mov_b64_e32 v[72:73], v[2:3]
	v_mov_b64_e32 v[74:75], v[2:3]
	v_mov_b64_e32 v[76:77], v[2:3]
	v_mov_b64_e32 v[78:79], v[2:3]
	v_mov_b64_e32 v[80:81], v[2:3]
	v_mov_b64_e32 v[82:83], v[2:3]
	v_mov_b64_e32 v[84:85], v[2:3]
	v_mov_b64_e32 v[86:87], v[2:3]
	v_mov_b64_e32 v[88:89], v[2:3]
	v_mov_b64_e32 v[90:91], v[2:3]
	v_mov_b64_e32 v[92:93], v[2:3]
	v_mov_b64_e32 v[94:95], v[2:3]
	v_mov_b64_e32 v[96:97], v[2:3]
	v_mov_b64_e32 v[98:99], v[2:3]
	v_mov_b64_e32 v[100:101], v[2:3]
	v_mov_b64_e32 v[102:103], v[2:3]
	v_mov_b64_e32 v[104:105], v[2:3]
	v_mov_b64_e32 v[106:107], v[2:3]
	v_mov_b64_e32 v[108:109], v[2:3]
	v_mov_b64_e32 v[110:111], v[2:3]
	v_mov_b64_e32 v[112:113], v[2:3]
	v_mov_b64_e32 v[114:115], v[2:3]
	v_mov_b64_e32 v[116:117], v[2:3]
	v_mov_b64_e32 v[118:119], v[2:3]
	v_mov_b64_e32 v[120:121], v[2:3]
	v_mov_b64_e32 v[122:123], v[2:3]
	v_mov_b64_e32 v[124:125], v[2:3]
	v_mov_b64_e32 v[126:127], v[2:3]
	v_mov_b64_e32 v[128:129], v[2:3]

.LBB0_1212:
	s_ashr_i32 s44, s62, 2
	s_ashr_i32 s45, s44, 31
	s_lshl_b64 s[44:45], s[44:45], 20
	s_add_u32 s37, s31, s44
	s_addc_u32 s44, s34, s45
	s_add_u32 s29, s37, s29
	s_addc_u32 s37, s44, s81
	s_add_u32 s44, s29, 0x800
	s_addc_u32 s45, s37, 0
	s_and_b64 s[48:49], s[16:17], exec
	v_mov_b32_e32 v2, 0
	s_cselect_b32 s37, s45, s39
	s_cselect_b32 s29, s44, s38
	s_mov_b64 s[52:53], 0
	s_mov_b64 s[48:49], -1
	s_mov_b64 s[50:51], 0
	v_mov_b32_e32 v3, v2
	v_mov_b64_e32 v[4:5], v[2:3]
	v_mov_b64_e32 v[6:7], v[2:3]
	v_mov_b64_e32 v[8:9], v[2:3]
	v_mov_b64_e32 v[10:11], v[2:3]
	v_mov_b64_e32 v[12:13], v[2:3]
	v_mov_b64_e32 v[14:15], v[2:3]
	v_mov_b64_e32 v[16:17], v[2:3]
	v_mov_b64_e32 v[18:19], v[2:3]
	v_mov_b64_e32 v[20:21], v[2:3]
	v_mov_b64_e32 v[22:23], v[2:3]
	v_mov_b64_e32 v[24:25], v[2:3]
	v_mov_b64_e32 v[26:27], v[2:3]
	v_mov_b64_e32 v[28:29], v[2:3]
	v_mov_b64_e32 v[30:31], v[2:3]
	v_mov_b64_e32 v[32:33], v[2:3]
	v_mov_b64_e32 v[34:35], v[2:3]
	v_mov_b64_e32 v[36:37], v[2:3]
	v_mov_b64_e32 v[38:39], v[2:3]
	v_mov_b64_e32 v[40:41], v[2:3]
	v_mov_b64_e32 v[42:43], v[2:3]
	v_mov_b64_e32 v[44:45], v[2:3]
	v_mov_b64_e32 v[46:47], v[2:3]
	v_mov_b64_e32 v[48:49], v[2:3]
	v_mov_b64_e32 v[50:51], v[2:3]
	v_mov_b64_e32 v[52:53], v[2:3]
	v_mov_b64_e32 v[54:55], v[2:3]
	v_mov_b64_e32 v[56:57], v[2:3]
	v_mov_b64_e32 v[58:59], v[2:3]
	v_mov_b64_e32 v[60:61], v[2:3]
	v_mov_b64_e32 v[62:63], v[2:3]
	v_mov_b64_e32 v[64:65], v[2:3]
	v_mov_b64_e32 v[66:67], v[2:3]
	v_mov_b64_e32 v[68:69], v[2:3]
	v_mov_b64_e32 v[70:71], v[2:3]
	v_mov_b64_e32 v[72:73], v[2:3]
	v_mov_b64_e32 v[74:75], v[2:3]
	v_mov_b64_e32 v[76:77], v[2:3]
	v_mov_b64_e32 v[78:79], v[2:3]
	v_mov_b64_e32 v[80:81], v[2:3]
	v_mov_b64_e32 v[82:83], v[2:3]
	v_mov_b64_e32 v[84:85], v[2:3]
	v_mov_b64_e32 v[86:87], v[2:3]
	v_mov_b64_e32 v[88:89], v[2:3]
	v_mov_b64_e32 v[90:91], v[2:3]
	v_mov_b64_e32 v[92:93], v[2:3]
	v_mov_b64_e32 v[94:95], v[2:3]
	v_mov_b64_e32 v[96:97], v[2:3]
	v_mov_b64_e32 v[98:99], v[2:3]
	v_mov_b64_e32 v[100:101], v[2:3]
	v_mov_b64_e32 v[102:103], v[2:3]
	v_mov_b64_e32 v[104:105], v[2:3]
	v_mov_b64_e32 v[106:107], v[2:3]
	v_mov_b64_e32 v[108:109], v[2:3]
	v_mov_b64_e32 v[110:111], v[2:3]
	v_mov_b64_e32 v[112:113], v[2:3]
	v_mov_b64_e32 v[114:115], v[2:3]
	v_mov_b64_e32 v[116:117], v[2:3]
	v_mov_b64_e32 v[118:119], v[2:3]
	v_mov_b64_e32 v[120:121], v[2:3]
	v_mov_b64_e32 v[122:123], v[2:3]
	v_mov_b64_e32 v[124:125], v[2:3]
	v_mov_b64_e32 v[126:127], v[2:3]
	v_mov_b64_e32 v[128:129], v[2:3]

.LBB0_2005:
	s_ashr_i32 s47, s46, 31
	s_lshl_b64 s[52:53], s[46:47], 19
	v_readlane_b32 s40, v253, 34
	v_readlane_b32 s41, v253, 35
	s_add_u32 s52, s40, s52
	s_addc_u32 s53, s41, s53
	s_and_b64 s[56:57], s[54:55], exec
	s_cselect_b32 s29, s53, s37
	s_cselect_b32 s47, s52, s36
	s_ashr_i32 s49, s48, 31
	s_lshl_b64 s[56:57], s[48:49], 19
	s_add_u32 s56, s35, s56
	s_addc_u32 s57, s64, s57
	s_and_b64 s[62:63], s[54:55], exec
	s_cselect_b32 s49, s57, s61
	s_cselect_b32 s59, s56, s60
	s_add_u32 s36, s36, 0x40080
	s_addc_u32 s37, s37, 0
	s_add_u32 s80, s60, 0x100
	v_mov_b32_e32 v2, 0
	s_addc_u32 s95, s61, 0
	s_mov_b32 vcc_lo, -2
	v_mov_b32_e32 v3, v2
	v_mov_b64_e32 v[4:5], v[2:3]
	v_mov_b64_e32 v[6:7], v[2:3]
	v_mov_b64_e32 v[8:9], v[2:3]
	v_mov_b64_e32 v[10:11], v[2:3]
	v_mov_b64_e32 v[12:13], v[2:3]
	v_mov_b64_e32 v[14:15], v[2:3]
	v_mov_b64_e32 v[16:17], v[2:3]
	v_mov_b64_e32 v[18:19], v[2:3]
	v_mov_b64_e32 v[20:21], v[2:3]
	v_mov_b64_e32 v[22:23], v[2:3]
	v_mov_b64_e32 v[24:25], v[2:3]
	v_mov_b64_e32 v[26:27], v[2:3]
	v_mov_b64_e32 v[28:29], v[2:3]
	v_mov_b64_e32 v[30:31], v[2:3]
	v_mov_b64_e32 v[32:33], v[2:3]
	v_mov_b64_e32 v[34:35], v[2:3]
	v_mov_b64_e32 v[36:37], v[2:3]
	v_mov_b64_e32 v[38:39], v[2:3]
	v_mov_b64_e32 v[40:41], v[2:3]
	v_mov_b64_e32 v[42:43], v[2:3]
	v_mov_b64_e32 v[44:45], v[2:3]
	v_mov_b64_e32 v[46:47], v[2:3]
	v_mov_b64_e32 v[48:49], v[2:3]
	v_mov_b64_e32 v[50:51], v[2:3]
	v_mov_b64_e32 v[52:53], v[2:3]
	v_mov_b64_e32 v[54:55], v[2:3]
	v_mov_b64_e32 v[56:57], v[2:3]
	v_mov_b64_e32 v[58:59], v[2:3]
	v_mov_b64_e32 v[60:61], v[2:3]
	v_mov_b64_e32 v[62:63], v[2:3]
	v_mov_b64_e32 v[64:65], v[2:3]
	v_mov_b64_e32 v[66:67], v[2:3]
	v_mov_b64_e32 v[68:69], v[2:3]
	v_mov_b64_e32 v[70:71], v[2:3]
	v_mov_b64_e32 v[72:73], v[2:3]
	v_mov_b64_e32 v[74:75], v[2:3]
	v_mov_b64_e32 v[76:77], v[2:3]
	v_mov_b64_e32 v[78:79], v[2:3]
	v_mov_b64_e32 v[80:81], v[2:3]
	v_mov_b64_e32 v[82:83], v[2:3]
	v_mov_b64_e32 v[84:85], v[2:3]
	v_mov_b64_e32 v[86:87], v[2:3]
	v_mov_b64_e32 v[88:89], v[2:3]
	v_mov_b64_e32 v[90:91], v[2:3]
	v_mov_b64_e32 v[92:93], v[2:3]
	v_mov_b64_e32 v[94:95], v[2:3]
	v_mov_b64_e32 v[96:97], v[2:3]
	v_mov_b64_e32 v[98:99], v[2:3]
	v_mov_b64_e32 v[100:101], v[2:3]
	v_mov_b64_e32 v[102:103], v[2:3]
	v_mov_b64_e32 v[104:105], v[2:3]
	v_mov_b64_e32 v[106:107], v[2:3]
	v_mov_b64_e32 v[108:109], v[2:3]
	v_mov_b64_e32 v[110:111], v[2:3]
	v_mov_b64_e32 v[112:113], v[2:3]
	v_mov_b64_e32 v[114:115], v[2:3]
	v_mov_b64_e32 v[116:117], v[2:3]
	v_mov_b64_e32 v[118:119], v[2:3]
	v_mov_b64_e32 v[120:121], v[2:3]
	v_mov_b64_e32 v[122:123], v[2:3]
	v_mov_b64_e32 v[124:125], v[2:3]
	v_mov_b64_e32 v[126:127], v[2:3]
	v_mov_b64_e32 v[128:129], v[2:3]

.LBB0_2066:
	s_add_u32 s52, s52, 0x40080
	s_addc_u32 s53, s53, 0
	s_add_u32 s17, s54, 0x100
	v_mov_b32_e32 v2, 0
	s_addc_u32 s29, s55, 0
	s_mov_b32 s39, -2
	v_mov_b32_e32 v3, v2
	v_mov_b64_e32 v[4:5], v[2:3]
	v_mov_b64_e32 v[6:7], v[2:3]
	v_mov_b64_e32 v[8:9], v[2:3]
	v_mov_b64_e32 v[10:11], v[2:3]
	v_mov_b64_e32 v[12:13], v[2:3]
	v_mov_b64_e32 v[14:15], v[2:3]
	v_mov_b64_e32 v[16:17], v[2:3]
	v_mov_b64_e32 v[18:19], v[2:3]
	v_mov_b64_e32 v[20:21], v[2:3]
	v_mov_b64_e32 v[22:23], v[2:3]
	v_mov_b64_e32 v[24:25], v[2:3]
	v_mov_b64_e32 v[26:27], v[2:3]
	v_mov_b64_e32 v[28:29], v[2:3]
	v_mov_b64_e32 v[30:31], v[2:3]
	v_mov_b64_e32 v[32:33], v[2:3]
	v_mov_b64_e32 v[34:35], v[2:3]
	v_mov_b64_e32 v[36:37], v[2:3]
	v_mov_b64_e32 v[38:39], v[2:3]
	v_mov_b64_e32 v[40:41], v[2:3]
	v_mov_b64_e32 v[42:43], v[2:3]
	v_mov_b64_e32 v[44:45], v[2:3]
	v_mov_b64_e32 v[46:47], v[2:3]
	v_mov_b64_e32 v[48:49], v[2:3]
	v_mov_b64_e32 v[50:51], v[2:3]
	v_mov_b64_e32 v[52:53], v[2:3]
	v_mov_b64_e32 v[54:55], v[2:3]
	v_mov_b64_e32 v[56:57], v[2:3]
	v_mov_b64_e32 v[58:59], v[2:3]
	v_mov_b64_e32 v[60:61], v[2:3]
	v_mov_b64_e32 v[62:63], v[2:3]
	v_mov_b64_e32 v[64:65], v[2:3]
	v_mov_b64_e32 v[66:67], v[2:3]
	v_mov_b64_e32 v[68:69], v[2:3]
	v_mov_b64_e32 v[70:71], v[2:3]
	v_mov_b64_e32 v[72:73], v[2:3]
	v_mov_b64_e32 v[74:75], v[2:3]
	v_mov_b64_e32 v[76:77], v[2:3]
	v_mov_b64_e32 v[78:79], v[2:3]
	v_mov_b64_e32 v[80:81], v[2:3]
	v_mov_b64_e32 v[82:83], v[2:3]
	v_mov_b64_e32 v[84:85], v[2:3]
	v_mov_b64_e32 v[86:87], v[2:3]
	v_mov_b64_e32 v[88:89], v[2:3]
	v_mov_b64_e32 v[90:91], v[2:3]
	v_mov_b64_e32 v[92:93], v[2:3]
	v_mov_b64_e32 v[94:95], v[2:3]
	v_mov_b64_e32 v[96:97], v[2:3]
	v_mov_b64_e32 v[98:99], v[2:3]
	v_mov_b64_e32 v[100:101], v[2:3]
	v_mov_b64_e32 v[102:103], v[2:3]
	v_mov_b64_e32 v[104:105], v[2:3]
	v_mov_b64_e32 v[106:107], v[2:3]
	v_mov_b64_e32 v[108:109], v[2:3]
	v_mov_b64_e32 v[110:111], v[2:3]
	v_mov_b64_e32 v[112:113], v[2:3]
	v_mov_b64_e32 v[114:115], v[2:3]
	v_mov_b64_e32 v[116:117], v[2:3]
	v_mov_b64_e32 v[118:119], v[2:3]
	v_mov_b64_e32 v[120:121], v[2:3]
	v_mov_b64_e32 v[122:123], v[2:3]
	v_mov_b64_e32 v[124:125], v[2:3]
	v_mov_b64_e32 v[126:127], v[2:3]
	v_mov_b64_e32 v[128:129], v[2:3]
